# stacked exact micro-changes: P8/P9 prologue de-serialisation, expert-parallel tile table in P7, 8 mov+mul pairs merged in GDN a+b
# speedup vs baseline: 1.0062x; 1.0014x over previous
.LBB0_233:
	v_lshlrev_b32_e32 v68, 16, v182
	v_and_b32_e32 v69, 0xffff0000, v182
	v_lshlrev_b32_e32 v74, 16, v185
	v_and_b32_e32 v75, 0xffff0000, v185
	v_xor_b32_e32 v39, 32, v209
	v_add_u32_e32 v42, 64, v100
	v_cmp_lt_i32_e32 vcc, v39, v42
	v_lshlrev_b32_e32 v108, 16, v28
	v_and_b32_e32 v109, 0xffff0000, v28
	v_cndmask_b32_e32 v39, v209, v39, vcc
	v_lshlrev_b32_e32 v105, 2, v39
	v_xor_b32_e32 v39, 16, v209
	v_cmp_lt_i32_e32 vcc, v39, v42
	v_lshlrev_b32_e32 v85, 16, v183
	v_and_b32_e32 v81, 0xffff0000, v183
	v_cndmask_b32_e32 v39, v209, v39, vcc
	v_lshlrev_b32_e32 v103, 2, v39
	v_xor_b32_e32 v39, 8, v209
	v_cmp_lt_i32_e32 vcc, v39, v42
	v_lshlrev_b32_e32 v78, 16, v184
	v_and_b32_e32 v79, 0xffff0000, v184
	v_cndmask_b32_e32 v39, v209, v39, vcc
	v_lshlrev_b32_e32 v102, 2, v39
	v_xor_b32_e32 v39, 4, v209
	v_cmp_lt_i32_e32 vcc, v39, v42
	v_lshlrev_b32_e32 v40, 16, v202
	v_and_b32_e32 v41, 0xffff0000, v202
	v_cndmask_b32_e32 v39, v209, v39, vcc
	v_lshlrev_b32_e32 v101, 2, v39
	v_xor_b32_e32 v39, 2, v209
	v_cmp_lt_i32_e32 vcc, v39, v42
	v_lshl_add_u32 v97, v38, 1, 0
	v_bitop3_b32 v38, v215, s82, 7 bitop3:0x6c
	v_cndmask_b32_e32 v39, v209, v39, vcc
	v_lshlrev_b32_e32 v100, 2, v39
	v_xor_b32_e32 v39, 1, v209
	v_cmp_lt_i32_e32 vcc, v39, v42
	v_lshlrev_b32_e32 v116, 16, v32
	v_and_b32_e32 v117, 0xffff0000, v32
	v_cndmask_b32_e32 v39, v209, v39, vcc
	v_lshlrev_b32_e32 v84, 16, v36
	v_and_b32_e32 v91, 0xffff0000, v36
	v_lshlrev_b32_e32 v58, 16, v35
	v_and_b32_e32 v59, 0xffff0000, v35
	v_lshlrev_b32_e32 v66, 16, v181
	v_and_b32_e32 v67, 0xffff0000, v181
	v_lshlrev_b32_e32 v76, 16, v188
	v_and_b32_e32 v77, 0xffff0000, v188
	v_lshlrev_b32_e32 v54, 16, v190
	v_and_b32_e32 v55, 0xffff0000, v190
	v_lshlrev_b32_e32 v46, 16, v194
	v_and_b32_e32 v47, 0xffff0000, v194
	v_lshlrev_b32_e32 v34, 16, v196
	v_and_b32_e32 v35, 0xffff0000, v196
	v_lshlrev_b32_e32 v36, 16, v199
	v_and_b32_e32 v37, 0xffff0000, v199
	v_lshlrev_b32_e32 v52, 16, v203
	v_and_b32_e32 v53, 0xffff0000, v203
	v_lshlrev_b32_e32 v98, 2, v39
	v_lshlrev_b32_e32 v92, 3, v38
	v_pk_fma_f32 v[38:39], v[224:225], v[108:109], 0 op_sel_hi:[1,1,0]
	v_lshlrev_b32_e32 v62, 16, v30
	v_and_b32_e32 v63, 0xffff0000, v30
	v_pk_fma_f32 v[38:39], v[230:231], v[116:117], v[38:39]
	v_lshlrev_b32_e32 v106, 16, v27
	v_pk_fma_f32 v[38:39], v[238:239], v[62:63], v[38:39]
	v_and_b32_e32 v107, 0xffff0000, v27
	v_pk_fma_f32 v[38:39], v[244:245], v[68:69], v[38:39]
	v_lshlrev_b32_e32 v87, 16, v186
	v_and_b32_e32 v83, 0xffff0000, v186
	v_mul_f32_e32 v42, 0xbfb8aa3b, v38
	v_mul_f32_e32 v43, 0xbfb8aa3b, v39
	v_lshlrev_b32_e32 v114, 16, v31
	v_and_b32_e32 v115, 0xffff0000, v31
	v_lshlrev_b32_e32 v72, 16, v187
	v_and_b32_e32 v73, 0xffff0000, v187
	v_lshlrev_b32_e32 v70, 16, v189
	v_and_b32_e32 v64, 0xffff0000, v189
	v_exp_f32_e32 v42, v42
	v_exp_f32_e32 v43, v43
	v_pk_fma_f32 v[44:45], v[222:223], v[106:107], 0 op_sel_hi:[1,1,0]
	v_lshlrev_b32_e32 v112, 16, v29
	v_pk_fma_f32 v[44:45], v[228:229], v[114:115], v[44:45]
	v_and_b32_e32 v88, 0xffff0000, v29
	v_pk_fma_f32 v[44:45], v[234:235], v[58:59], v[44:45]
	v_lshlrev_b32_e32 v71, 16, v192
	v_pk_fma_f32 v[44:45], v[242:243], v[66:67], v[44:45]
	v_and_b32_e32 v65, 0xffff0000, v192
	v_lshlrev_b32_e32 v60, 16, v191
	v_and_b32_e32 v61, 0xffff0000, v191
	v_lshlrev_b32_e32 v29, 16, v198
	v_and_b32_e32 v25, 0xffff0000, v198
	v_lshlrev_b32_e32 v48, 16, v197
	v_and_b32_e32 v49, 0xffff0000, v197
	v_add_f32_e32 v42, 1.0, v42
	v_add_f32_e32 v43, 1.0, v43
	v_mul_f32_e32 v56, 0xbfb8aa3b, v44
	v_mul_f32_e32 v57, 0xbfb8aa3b, v45
	v_rcp_f32_e32 v42, v42
	v_rcp_f32_e32 v43, v43
	v_exp_f32_e32 v56, v56
	v_exp_f32_e32 v57, v57
	v_lshlrev_b32_e32 v113, 16, v33
	v_pk_mul_f32 v[38:39], v[38:39], v[42:43]
	v_add_f32_e32 v42, 1.0, v56
	v_add_f32_e32 v43, 1.0, v57
	v_rcp_f32_e32 v42, v42
	v_rcp_f32_e32 v43, v43
	v_pk_mul_f32 v[56:57], v[38:39], v[38:39]
	v_mov_b32_e32 v86, v85
	v_add_f32_e32 v119, v56, v57
	v_pk_mul_f32 v[44:45], v[44:45], v[42:43]
	v_pk_fma_f32 v[42:43], v[224:225], v[116:117], 0 op_sel_hi:[1,1,0]
	s_waitcnt lgkmcnt(0)
	v_mul_f32_e32 v24, 0xbfb8aa3b, v205
	v_pk_fma_f32 v[42:43], v[230:231], v[62:63], v[42:43]
	v_exp_f32_e32 v24, v24
	v_pk_fma_f32 v[42:43], v[238:239], v[68:69], v[42:43]
	v_and_b32_e32 v89, 0xffff0000, v33
	v_pk_fma_f32 v[42:43], v[244:245], v[74:75], v[42:43]
	v_add_f32_e32 v24, 1.0, v24
	v_mul_f32_e32 v56, 0xbfb8aa3b, v42
	v_exp_f32_e32 v106, v56
	v_mul_f32_e32 v56, 0xbfb8aa3b, v43
	v_exp_f32_e32 v107, v56
	v_pk_mul_f32 v[56:57], v[44:45], v[44:45]
	v_add_f32_e32 v106, 1.0, v106
	v_rcp_f32_e32 v106, v106
	v_add_f32_e32 v107, 1.0, v107
	v_rcp_f32_e32 v107, v107
	v_add_f32_e32 v116, v56, v57
	v_rcp_f32_e32 v95, v24
	v_mov_b32_e32 v90, v89
	v_pk_mul_f32 v[42:43], v[42:43], v[106:107]
	v_pk_fma_f32 v[88:89], v[226:227], v[88:89], 0 op_sel:[1,0,0] op_sel_hi:[1,1,0]
	v_pk_mul_f32 v[56:57], v[42:43], v[42:43]
	v_mov_b32_e32 v80, v91
	v_add_f32_e32 v117, v56, v57
	v_pk_fma_f32 v[56:57], v[222:223], v[114:115], 0 op_sel_hi:[1,1,0]
	v_mov_b32_e32 v114, v113
	v_pk_fma_f32 v[56:57], v[228:229], v[58:59], v[56:57]
	v_mov_b32_e32 v115, v84
	v_pk_fma_f32 v[56:57], v[234:235], v[66:67], v[56:57]
	v_pk_fma_f32 v[112:113], v[226:227], v[112:113], 0 op_sel_hi:[0,1,0]
	v_pk_fma_f32 v[56:57], v[242:243], v[78:79], v[56:57]
	v_pk_fma_f32 v[112:113], v[232:233], v[114:115], v[112:113] op_sel_hi:[0,1,1]
	v_mul_f32_e32 v106, 0xbfb8aa3b, v56
	v_exp_f32_e32 v107, v106
	v_mul_f32_e32 v106, 0xbfb8aa3b, v57
	v_exp_f32_e32 v109, v106
	v_pk_fma_f32 v[112:113], v[240:241], v[84:85], v[112:113] op_sel_hi:[0,1,1]
	v_add_f32_e32 v107, 1.0, v107
	v_pk_fma_f32 v[112:113], v[246:247], v[86:87], v[112:113] op_sel_hi:[0,1,1]
	v_rcp_f32_e32 v108, v107
	v_add_f32_e32 v107, 1.0, v109
	v_mul_f32_e32 v109, 0xbfb8aa3b, v112
	v_exp_f32_e32 v110, v109
	v_mul_f32_e32 v109, 0xbfb8aa3b, v113
	v_exp_f32_e32 v115, v109
	v_rcp_f32_e32 v109, v107
	v_add_f32_e32 v107, 1.0, v110
	v_rcp_f32_e32 v114, v107
	v_add_f32_e32 v107, 1.0, v115
	v_rcp_f32_e32 v115, v107
	v_pk_mul_f32 v[56:57], v[56:57], v[108:109]
	v_readlane_b32 s2, v95, s95
	v_pk_mul_f32 v[108:109], v[56:57], v[56:57]
	v_readlane_b32 s3, v95, s54
	v_add_f32_e32 v120, v108, v109
	v_pk_mul_f32 v[108:109], v[112:113], v[114:115]
	v_pk_fma_f32 v[88:89], v[232:233], v[90:91], v[88:89] op_sel:[1,0,0]
	v_mov_b32_e32 v82, v81
	v_pk_mul_f32 v[108:109], v[108:109], s[2:3]
	v_pk_fma_f32 v[88:89], v[240:241], v[80:81], v[88:89] op_sel:[1,0,0]
	v_cvt_pk_bf16_f32 v107, v108, v109
	v_pk_fma_f32 v[108:109], v[246:247], v[82:83], v[88:89] op_sel:[1,0,0]
	v_pk_fma_f32 v[62:63], v[224:225], v[62:63], 0 op_sel_hi:[1,1,0]
	v_mul_f32_e32 v88, 0xbfb8aa3b, v108
	v_exp_f32_e32 v88, v88
	v_mul_f32_e32 v89, 0xbfb8aa3b, v109
	v_exp_f32_e32 v89, v89
	v_pk_fma_f32 v[62:63], v[230:231], v[68:69], v[62:63]
	v_lshlrev_b32_e32 v32, 16, v193
	v_and_b32_e32 v33, 0xffff0000, v193
	v_lshlrev_b32_e32 v28, 16, v195
	v_and_b32_e32 v24, 0xffff0000, v195
	v_lshlrev_b32_e32 v50, 16, v200
	v_and_b32_e32 v51, 0xffff0000, v200
	v_mul_lo_u32 v93, v215, s11
	v_add_f32_e32 v88, 1.0, v88
	v_pk_fma_f32 v[62:63], v[238:239], v[74:75], v[62:63]
	v_add_lshl_u32 v90, v92, v93, 1
	v_rcp_f32_e32 v112, v88
	v_add_f32_e32 v88, 1.0, v89
	v_pk_fma_f32 v[62:63], v[244:245], v[76:77], v[62:63]
	v_rcp_f32_e32 v113, v88
	v_add_u32_e32 v88, 0, v90
	v_add_u32_e32 v91, s12, v90
	v_mul_f32_e32 v90, 0xbfb8aa3b, v62
	v_exp_f32_e32 v90, v90
	v_mul_f32_e32 v110, 0xbfb8aa3b, v63
	v_exp_f32_e32 v110, v110
	v_pk_fma_f32 v[58:59], v[222:223], v[58:59], 0 op_sel_hi:[1,1,0]
	v_add_f32_e32 v90, 1.0, v90
	v_pk_fma_f32 v[58:59], v[228:229], v[66:67], v[58:59]
	v_pk_mul_f32 v[108:109], v[108:109], v[112:113]
	v_pk_fma_f32 v[58:59], v[234:235], v[78:79], v[58:59]
	v_rcp_f32_e32 v112, v90
	v_pk_fma_f32 v[114:115], v[242:243], v[72:73], v[58:59]
	v_add_f32_e32 v90, 1.0, v110
	v_mul_f32_e32 v58, 0xbfb8aa3b, v114
	v_rcp_f32_e32 v113, v90
	v_exp_f32_e32 v90, v58
	v_mul_f32_e32 v58, 0xbfb8aa3b, v115
	v_exp_f32_e32 v110, v58
	v_pk_mul_f32 v[58:59], v[62:63], v[112:113]
	v_add_f32_e32 v62, 1.0, v90
	v_rcp_f32_e32 v62, v62
	v_add_f32_e32 v63, 1.0, v110
	v_rcp_f32_e32 v63, v63
	v_pk_fma_f32 v[68:69], v[224:225], v[68:69], 0 op_sel_hi:[1,1,0]
	v_pk_mul_f32 v[112:113], v[58:59], v[58:59]
	v_pk_fma_f32 v[68:69], v[230:231], v[74:75], v[68:69]
	v_pk_mul_f32 v[62:63], v[114:115], v[62:63]
	v_pk_fma_f32 v[68:69], v[238:239], v[76:77], v[68:69]
	v_add_f32_e32 v122, v112, v113
	v_pk_fma_f32 v[68:69], v[244:245], v[60:61], v[68:69]
	v_pk_mul_f32 v[112:113], v[62:63], v[62:63]
	v_mul_f32_e32 v110, 0xbfb8aa3b, v68
	v_add_f32_e32 v123, v112, v113
	v_exp_f32_e32 v110, v110
	v_mul_f32_e32 v112, 0xbfb8aa3b, v69
	v_exp_f32_e32 v113, v112
	v_pk_fma_f32 v[66:67], v[222:223], v[66:67], 0 op_sel_hi:[1,1,0]
	v_add_f32_e32 v110, 1.0, v110
	v_pk_fma_f32 v[66:67], v[228:229], v[78:79], v[66:67]
	v_rcp_f32_e32 v112, v110
	v_pk_fma_f32 v[66:67], v[234:235], v[72:73], v[66:67]
	v_add_f32_e32 v110, 1.0, v113
	v_pk_fma_f32 v[114:115], v[242:243], v[54:55], v[66:67]
	v_rcp_f32_e32 v113, v110
	v_mul_f32_e32 v66, 0xbfb8aa3b, v114
	v_exp_f32_e32 v110, v66
	v_mul_f32_e32 v66, 0xbfb8aa3b, v115
	v_exp_f32_e32 v124, v66
	v_pk_mul_f32 v[66:67], v[68:69], v[112:113]
	v_add_f32_e32 v68, 1.0, v110
	v_pk_mul_f32 v[112:113], v[66:67], v[66:67]
	v_add_f32_e32 v69, 1.0, v124
	v_pk_fma_f32 v[84:85], v[226:227], v[84:85], 0 op_sel_hi:[0,1,0]
	v_rcp_f32_e32 v68, v68
	v_rcp_f32_e32 v69, v69
	v_add_f32_e32 v124, v112, v113
	v_pk_mov_b32 v[112:113], v[86:87], v[70:71] op_sel:[1,0]
	v_pk_fma_f32 v[84:85], v[232:233], v[86:87], v[84:85] op_sel_hi:[0,1,1]
	v_pk_fma_f32 v[84:85], v[240:241], v[112:113], v[84:85] op_sel_hi:[0,1,1]
	v_pk_fma_f32 v[84:85], v[246:247], v[70:71], v[84:85] op_sel_hi:[0,1,1]
	v_mul_f32_e32 v86, 0xbfb8aa3b, v84
	v_pk_mul_f32 v[68:69], v[114:115], v[68:69]
	v_exp_f32_e32 v114, v86
	v_mul_f32_e32 v86, 0xbfb8aa3b, v85
	v_exp_f32_e32 v115, v86
	v_pk_mul_f32 v[86:87], v[68:69], v[68:69]
	v_add_f32_e32 v114, 1.0, v114
	v_pk_fma_f32 v[80:81], v[226:227], v[80:81], 0 op_sel:[1,0,0] op_sel_hi:[1,1,0]
	v_add_f32_e32 v115, 1.0, v115
	v_rcp_f32_e32 v114, v114
	v_rcp_f32_e32 v115, v115
	v_add_f32_e32 v125, v86, v87
	v_pk_mov_b32 v[86:87], v[82:83], v[64:65] op_sel:[1,0]
	v_pk_fma_f32 v[80:81], v[232:233], v[82:83], v[80:81] op_sel:[1,0,0]
	v_pk_mul_f32 v[84:85], v[84:85], v[114:115]
	v_pk_fma_f32 v[80:81], v[240:241], v[86:87], v[80:81] op_sel:[1,0,0]
	s_mul_i32 s1, s76, 0x12000
	v_pk_fma_f32 v[80:81], v[246:247], v[64:65], v[80:81] op_sel:[1,0,0]
	s_mul_hi_i32 s0, s76, 0x12000
	v_mul_f32_e32 v82, 0xbfb8aa3b, v80
	v_exp_f32_e32 v114, v82
	v_mul_f32_e32 v82, 0xbfb8aa3b, v81
	v_exp_f32_e32 v115, v82
	s_add_u32 s78, s40, s1
	s_addc_u32 s79, s41, s0
	s_mul_i32 s0, s82, 0x440
	v_readlane_b32 s82, v95, s55
	v_readlane_b32 s83, v95, s33
	v_pk_fma_f32 v[74:75], v[224:225], v[74:75], 0 op_sel_hi:[1,1,0]
	v_pk_fma_f32 v[78:79], v[222:223], v[78:79], 0 op_sel_hi:[1,1,0]
	v_pk_mul_f32 v[82:83], v[84:85], s[82:83]
	v_add_f32_e32 v84, 1.0, v114
	v_rcp_f32_e32 v114, v84
	v_add_f32_e32 v84, 1.0, v115
	v_rcp_f32_e32 v115, v84
	v_pk_fma_f32 v[74:75], v[230:231], v[76:77], v[74:75]
	v_cvt_pk_bf16_f32 v84, v82, v83
	v_pk_fma_f32 v[74:75], v[238:239], v[60:61], v[74:75]
	v_pk_mul_f32 v[80:81], v[80:81], v[114:115]
	v_pk_fma_f32 v[74:75], v[244:245], v[46:47], v[74:75]
	v_pk_mul_f32 v[80:81], v[80:81], s[82:83]
	v_mul_f32_e32 v82, 0xbfb8aa3b, v74
	v_mul_f32_e32 v114, 0xbfb8aa3b, v75
	v_exp_f32_e32 v82, v82
	v_exp_f32_e32 v114, v114
	v_cvt_pk_bf16_f32 v115, v80, v81
	v_pk_fma_f32 v[78:79], v[228:229], v[72:73], v[78:79]
	v_add_f32_e32 v80, 1.0, v82
	v_add_f32_e32 v81, 1.0, v114
	v_rcp_f32_e32 v80, v80
	v_rcp_f32_e32 v81, v81
	v_pk_fma_f32 v[78:79], v[234:235], v[54:55], v[78:79]
	v_and_b32_e32 v118, 32, v215
	v_pk_fma_f32 v[78:79], v[242:243], v[32:33], v[78:79]
	v_pk_mul_f32 v[74:75], v[74:75], v[80:81]
	v_cmp_eq_u32_e32 vcc, 0, v118
	v_pk_mul_f32 v[80:81], v[74:75], v[74:75]
	v_mul_f32_e32 v118, 0xbfb8aa3b, v79
	v_add_f32_e32 v80, v80, v81
	v_mul_f32_e32 v81, 0xbfb8aa3b, v78
	v_exp_f32_e32 v81, v81
	v_exp_f32_e32 v118, v118
	v_add_u32_e32 v89, 0x48, v93
	v_or_b32_e32 v126, 2, v92
	v_add_u32_e32 v83, v126, v89
	v_lshl_add_u32 v114, v83, 1, s12
	v_cndmask_b32_e32 v83, v80, v119, vcc
	v_cndmask_b32_e32 v80, v119, v80, vcc
	ds_bpermute_b32 v119, v105, v80
	v_add_f32_e32 v80, 1.0, v81
	v_add_f32_e32 v81, 1.0, v118
	v_rcp_f32_e32 v80, v80
	v_rcp_f32_e32 v81, v81
	v_pk_fma_f32 v[76:77], v[224:225], v[76:77], 0 op_sel_hi:[1,1,0]
	s_waitcnt lgkmcnt(0)
	v_add_f32_e32 v118, v83, v119
	v_pk_fma_f32 v[76:77], v[230:231], v[60:61], v[76:77]
	v_pk_mul_f32 v[78:79], v[78:79], v[80:81]
	v_pk_fma_f32 v[76:77], v[238:239], v[46:47], v[76:77]
	v_pk_mul_f32 v[80:81], v[78:79], v[78:79]
	v_pk_fma_f32 v[76:77], v[244:245], v[48:49], v[76:77]
	v_add_f32_e32 v80, v80, v81
	v_cndmask_b32_e32 v119, v80, v116, vcc
	v_cndmask_b32_e32 v80, v116, v80, vcc
	v_mul_f32_e32 v81, 0xbfb8aa3b, v76
	v_mul_f32_e32 v116, 0xbfb8aa3b, v77
	v_exp_f32_e32 v81, v81
	v_exp_f32_e32 v116, v116
	v_pk_mul_f32 v[108:109], v[108:109], s[2:3]
	v_add_lshl_u32 v121, v92, v89, 1
	v_cvt_pk_bf16_f32 v108, v108, v109
	v_add_u32_e32 v109, s12, v121
	v_add_u32_e32 v82, 0, v121
	ds_bpermute_b32 v121, v105, v80
	v_add_f32_e32 v80, 1.0, v81
	v_add_f32_e32 v81, 1.0, v116
	v_rcp_f32_e32 v80, v80
	v_rcp_f32_e32 v81, v81
	v_pk_fma_f32 v[72:73], v[222:223], v[72:73], 0 op_sel_hi:[1,1,0]
	s_waitcnt lgkmcnt(0)
	v_add_f32_e32 v116, v119, v121
	v_pk_fma_f32 v[72:73], v[228:229], v[54:55], v[72:73]
	v_pk_mul_f32 v[76:77], v[76:77], v[80:81]
	v_pk_fma_f32 v[72:73], v[234:235], v[32:33], v[72:73]
	v_pk_mul_f32 v[80:81], v[76:77], v[76:77]
	v_pk_fma_f32 v[72:73], v[242:243], v[34:35], v[72:73]
	v_add_f32_e32 v119, v80, v81
	v_mul_f32_e32 v81, 0xbfb8aa3b, v72
	v_mul_f32_e32 v121, 0xbfb8aa3b, v73
	v_exp_f32_e32 v81, v81
	v_exp_f32_e32 v121, v121
	v_cndmask_b32_e32 v80, v117, v119, vcc
	v_add_u32_e32 v127, v126, v93
	ds_bpermute_b32 v126, v105, v80
	v_add_f32_e32 v80, 1.0, v81
	v_add_f32_e32 v81, 1.0, v121
	v_rcp_f32_e32 v80, v80
	v_rcp_f32_e32 v81, v81
	v_pk_fma_f32 v[112:113], v[226:227], v[112:113], 0 op_sel_hi:[0,1,0]
	v_cndmask_b32_e32 v117, v119, v117, vcc
	s_waitcnt lgkmcnt(0)
	v_add_f32_e32 v117, v117, v126
	v_pk_mul_f32 v[80:81], v[72:73], v[80:81]
	v_pk_fma_f32 v[60:61], v[224:225], v[60:61], 0 op_sel_hi:[1,1,0]
	v_pk_mul_f32 v[72:73], v[80:81], v[80:81]
	v_pk_fma_f32 v[60:61], v[230:231], v[46:47], v[60:61]
	v_add_f32_e32 v72, v72, v73
	v_cndmask_b32_e32 v121, v72, v120, vcc
	v_cndmask_b32_e32 v120, v120, v72, vcc
	v_pk_mov_b32 v[72:73], v[70:71], v[28:29] op_sel:[1,0]
	v_pk_fma_f32 v[70:71], v[232:233], v[70:71], v[112:113] op_sel_hi:[0,1,1]
	v_pk_fma_f32 v[70:71], v[240:241], v[72:73], v[70:71] op_sel_hi:[0,1,1]
	v_pk_fma_f32 v[70:71], v[246:247], v[28:29], v[70:71] op_sel_hi:[0,1,1]
	v_mul_f32_e32 v112, 0xbfb8aa3b, v71
	v_exp_f32_e32 v112, v112
	v_mul_f32_e32 v113, 0xbfb8aa3b, v70
	v_exp_f32_e32 v126, v113
	v_pk_fma_f32 v[60:61], v[238:239], v[48:49], v[60:61]
	v_add_f32_e32 v112, 1.0, v112
	v_rcp_f32_e32 v113, v112
	v_add_f32_e32 v112, 1.0, v126
	v_rcp_f32_e32 v112, v112
	v_readlane_b32 s92, v95, s4
	v_readlane_b32 s93, v95, s5
	v_pk_fma_f32 v[86:87], v[226:227], v[86:87], 0 op_sel:[1,0,0] op_sel_hi:[1,1,0]
	v_pk_mul_f32 v[70:71], v[70:71], v[112:113]
	v_pk_fma_f32 v[60:61], v[244:245], v[50:51], v[60:61]
	v_pk_mul_f32 v[112:113], v[70:71], s[92:93]
	v_pk_mov_b32 v[70:71], v[64:65], v[24:25] op_sel:[1,0]
	v_pk_fma_f32 v[64:65], v[232:233], v[64:65], v[86:87] op_sel:[1,0,0]
	v_mul_f32_e32 v86, 0xbfb8aa3b, v60
	v_mul_f32_e32 v87, 0xbfb8aa3b, v61
	v_exp_f32_e32 v86, v86
	v_exp_f32_e32 v87, v87
	v_pk_fma_f32 v[54:55], v[222:223], v[54:55], 0 op_sel_hi:[1,1,0]
	v_pk_fma_f32 v[16:17], v[224:225], v[46:47], 0 op_sel_hi:[1,1,0]
	v_add_f32_e32 v86, 1.0, v86
	v_add_f32_e32 v87, 1.0, v87
	v_rcp_f32_e32 v86, v86
	v_rcp_f32_e32 v87, v87
	v_pk_fma_f32 v[8:9], v[222:223], v[32:33], 0 op_sel_hi:[1,1,0]
	v_pk_fma_f32 v[54:55], v[228:229], v[32:33], v[54:55]
	v_pk_fma_f32 v[16:17], v[230:231], v[48:49], v[16:17]
	v_pk_mul_f32 v[60:61], v[60:61], v[86:87]
	v_pk_fma_f32 v[8:9], v[228:229], v[34:35], v[8:9]
	v_pk_mul_f32 v[86:87], v[60:61], v[60:61]
	v_pk_fma_f32 v[54:55], v[234:235], v[34:35], v[54:55]
	v_add_f32_e32 v86, v86, v87
	v_pk_fma_f32 v[16:17], v[238:239], v[50:51], v[16:17]
	v_pk_fma_f32 v[8:9], v[234:235], v[36:37], v[8:9]
	v_cndmask_b32_e32 v87, v122, v86, vcc
	v_pk_fma_f32 v[54:55], v[242:243], v[36:37], v[54:55]
	v_pk_fma_f32 v[16:17], v[244:245], v[52:53], v[16:17]
	v_pk_fma_f32 v[8:9], v[242:243], v[40:41], v[8:9]
	v_lshlrev_b32_e32 v30, 16, v201
	v_and_b32_e32 v26, 0xffff0000, v201
	v_lshl_add_u32 v96, s0, 1, v97
	s_mul_i32 s0, s54, 0x88
	ds_bpermute_b32 v128, v105, v87
	v_cvt_pk_bf16_f32 v129, v112, v113
	v_mul_f32_e32 v112, 0xbfb8aa3b, v54
	v_mul_f32_e32 v113, 0xbfb8aa3b, v55
	v_mul_f32_e32 v18, 0xbfb8aa3b, v16
	v_mul_f32_e32 v19, 0xbfb8aa3b, v17
	v_mul_f32_e32 v10, 0xbfb8aa3b, v8
	v_mul_f32_e32 v11, 0xbfb8aa3b, v9
	v_lshl_add_u32 v106, s0, 1, v97
	v_readlane_b32 s0, v253, 45
	v_exp_f32_e32 v112, v112
	v_exp_f32_e32 v113, v113
	v_exp_f32_e32 v18, v18
	v_exp_f32_e32 v19, v19
	v_exp_f32_e32 v10, v10
	v_exp_f32_e32 v11, v11
	v_lshl_add_u32 v90, s0, 1, v97
	v_readlane_b32 s0, v253, 46
	v_and_b32_e32 v111, 16, v215
	v_cndmask_b32_e32 v86, v86, v122, vcc
	v_lshl_add_u32 v110, s0, 1, v97
	v_readlane_b32 s0, v253, 47
	s_waitcnt lgkmcnt(0)
	v_add_f32_e32 v86, v86, v128
	v_add_f32_e32 v112, 1.0, v112
	v_lshl_add_u32 v83, s0, 1, v97
	v_readlane_b32 s0, v253, 48
	v_add_f32_e32 v113, 1.0, v113
	v_add_f32_e32 v18, 1.0, v18
	v_lshl_add_u32 v119, s0, 1, v97
	v_cmp_eq_u32_e64 s[0:1], 0, v111
	v_add_f32_e32 v19, 1.0, v19
	v_add_f32_e32 v10, 1.0, v10
	v_add_f32_e32 v11, 1.0, v11
	v_cndmask_b32_e64 v111, v86, v118, s[0:1]
	v_cndmask_b32_e64 v86, v118, v86, s[0:1]
	v_rcp_f32_e32 v112, v112
	v_rcp_f32_e32 v113, v113
	v_rcp_f32_e32 v18, v18
	v_rcp_f32_e32 v19, v19
	v_rcp_f32_e32 v10, v10
	v_rcp_f32_e32 v11, v11
	ds_bpermute_b32 v86, v103, v86
	v_pk_mul_f32 v[54:55], v[54:55], v[112:113]
	v_pk_mul_f32 v[16:17], v[16:17], v[18:19]
	v_pk_mul_f32 v[8:9], v[8:9], v[10:11]
	v_pk_mul_f32 v[112:113], v[54:55], v[54:55]
	v_pk_mul_f32 v[18:19], v[16:17], v[16:17]
	v_pk_mul_f32 v[10:11], v[8:9], v[8:9]
	s_waitcnt lgkmcnt(0)
	v_add_f32_e32 v86, v111, v86
	v_add_f32_e32 v111, v112, v113
	v_add_f32_e32 v18, v18, v19
	v_add_f32_e32 v10, v10, v11
	v_cndmask_b32_e32 v112, v111, v123, vcc
	v_cndmask_b32_e32 v111, v123, v111, vcc
	v_cndmask_b32_e32 v19, v18, v124, vcc
	v_cndmask_b32_e32 v18, v124, v18, vcc
	v_cndmask_b32_e32 v11, v125, v10, vcc
	ds_bpermute_b32 v120, v105, v120
	ds_bpermute_b32 v111, v105, v111
	ds_bpermute_b32 v12, v105, v18
	ds_bpermute_b32 v11, v105, v11
	v_cndmask_b32_e32 v10, v10, v125, vcc
	s_waitcnt lgkmcnt(3)
	v_add_f32_e32 v120, v121, v120
	s_waitcnt lgkmcnt(2)
	v_add_f32_e32 v20, v112, v111
	s_waitcnt lgkmcnt(1)
	v_add_f32_e32 v12, v19, v12
	s_waitcnt lgkmcnt(0)
	v_add_f32_e32 v10, v10, v11
	v_cndmask_b32_e64 v21, v20, v116, s[0:1]
	v_cndmask_b32_e64 v20, v116, v20, s[0:1]
	v_cndmask_b32_e64 v13, v117, v12, s[0:1]
	v_cndmask_b32_e64 v11, v120, v10, s[0:1]
	ds_bpermute_b32 v20, v103, v20
	ds_bpermute_b32 v13, v103, v13
	ds_bpermute_b32 v11, v103, v11
	v_and_b32_e32 v104, 8, v215
	v_cndmask_b32_e64 v12, v12, v117, s[0:1]
	v_cndmask_b32_e64 v10, v10, v120, s[0:1]
	s_waitcnt lgkmcnt(2)
	v_add_f32_e32 v14, v21, v20
	s_waitcnt lgkmcnt(1)
	v_add_f32_e32 v12, v12, v13
	v_cmp_eq_u32_e32 vcc, 0, v104
	s_waitcnt lgkmcnt(0)
	v_add_f32_e32 v10, v10, v11
	v_lshlrev_b32_e32 v31, 16, v204
	v_cndmask_b32_e32 v13, v12, v86, vcc
	v_cndmask_b32_e32 v12, v86, v12, vcc
	v_cndmask_b32_e32 v11, v14, v10, vcc
	ds_bpermute_b32 v12, v102, v12
	ds_bpermute_b32 v11, v102, v11
	v_and_b32_e32 v27, 0xffff0000, v204
	v_and_b32_e32 v99, 4, v215
	v_pk_fma_f32 v[64:65], v[240:241], v[70:71], v[64:65] op_sel:[1,0,0]
	v_cndmask_b32_e32 v10, v10, v14, vcc
	v_pk_fma_f32 v[64:65], v[246:247], v[24:25], v[64:65] op_sel:[1,0,0]
	s_waitcnt lgkmcnt(1)
	v_add_f32_e32 v12, v13, v12
	s_waitcnt lgkmcnt(0)
	v_add_f32_e32 v10, v10, v11
	v_cmp_eq_u32_e32 vcc, 0, v99
	v_lshl_add_u32 v85, v127, 1, s12
	v_mul_f32_e32 v127, 0xbfb8aa3b, v65
	v_mul_f32_e32 v118, 0xbfb8aa3b, v64
	v_cndmask_b32_e32 v13, v12, v10, vcc
	v_cndmask_b32_e32 v10, v10, v12, vcc
	v_exp_f32_e32 v127, v127
	v_exp_f32_e32 v118, v118
	ds_bpermute_b32 v12, v101, v10
	v_readlane_b32 s0, v253, 49
	v_add_f32_e32 v87, 1.0, v127
	v_add_f32_e32 v15, 1.0, v118
	v_rcp_f32_e32 v87, v87
	v_rcp_f32_e32 v86, v15
	s_waitcnt lgkmcnt(0)
	v_add_f32_e32 v12, v13, v12
	ds_bpermute_b32 v13, v100, v12
	v_lshl_add_u32 v33, s0, 1, v97
	v_pk_mul_f32 v[10:11], v[64:65], v[86:87]
	v_readlane_b32 s0, v253, 50
	v_pk_mul_f32 v[10:11], v[10:11], s[92:93]
	s_mov_b32 s74, 0x358637bd
	v_cvt_pk_bf16_f32 v23, v10, v11
	s_waitcnt lgkmcnt(0)
	v_add_f32_e32 v10, v12, v13
	ds_bpermute_b32 v11, v98, v10
	v_or_b32_e32 v121, 4, v92
	v_lshl_add_u32 v34, s0, 1, v97
	v_add_u32_e32 v14, v121, v89
	v_lshl_add_u32 v32, v14, 1, s12
	s_waitcnt lgkmcnt(0)
	v_add_f32_e32 v35, v10, v11
	v_mov_b64_e32 v[10:11], s[74:75]
	v_readlane_b32 s1, v35, 0
	v_readlane_b32 s0, v35, 4
	v_readlane_b32 s80, v94, s95
	v_readlane_b32 s81, v94, s54
	v_pk_add_f32 v[12:13], s[0:1], v[10:11] op_sel_hi:[1,0]
	v_readlane_b32 s20, v94, s55
	v_readlane_b32 s21, v94, s33
	v_rsq_f32_e32 v13, v13
	v_rsq_f32_e32 v14, v12
	v_mul_f32_e32 v12, 0x3db504f3, v13
	v_pk_mul_f32 v[12:13], v[44:45], v[12:13] op_sel_hi:[1,0]
	v_readlane_b32 s1, v35, 8
	v_cvt_pk_bf16_f32 v12, v12, v13
	v_readlane_b32 s0, v35, 12
	ds_write_b32 v96, v12 offset:34816
	v_pk_mul_f32 v[14:15], v[38:39], v[14:15] op_sel_hi:[1,0]
	v_pk_add_f32 v[12:13], s[0:1], v[10:11] op_sel_hi:[1,0]
	v_cvt_pk_bf16_f32 v36, v14, v15
	v_readlane_b32 s22, v94, s4
	v_rsq_f32_e32 v13, v13
	v_rsq_f32_e32 v18, v12
	v_mul_f32_e32 v12, 0x3db504f3, v13
	v_pk_mul_f32 v[12:13], v[56:57], v[12:13] op_sel_hi:[1,0]
	v_pk_mul_f32 v[18:19], v[42:43], v[18:19] op_sel_hi:[1,0]
	v_cvt_pk_bf16_f32 v12, v12, v13
	v_cvt_pk_bf16_f32 v37, v18, v19
	ds_write_b32 v106, v12 offset:34816
	v_mov_b32_e32 v12, v14
	v_mov_b32_e32 v13, v18
	v_mov_b32_e32 v18, v15
	v_pk_mul_f32 v[12:13], s[2:3], v[12:13]
	v_pk_mul_f32 v[14:15], s[2:3], v[18:19]
	v_pk_mul_f32 v[20:21], s[80:81], v[12:13]
	v_cvt_pk_bf16_f32 v12, v12, v14
	v_pk_mul_f32 v[18:19], s[80:81], v[14:15]
	ds_write2st64_b32 v96, v36, v12 offset1:68
	v_cvt_pk_bf16_f32 v12, v13, v15
	v_cvt_pk_bf16_f32 v20, v20, v21
	ds_write2st64_b32 v106, v37, v12 offset1:68
	ds_write_b32 v88, v107 offset:52224
	ds_write_b32 v91, v20
	ds_write_b32 v88, v108 offset:52368
	v_cvt_pk_bf16_f32 v12, v18, v19
	v_readlane_b32 s1, v35, 16
	v_readlane_b32 s0, v35, 20
	ds_write_b32 v109, v12
	v_readlane_b32 s23, v94, s5
	v_pk_add_f32 v[12:13], s[0:1], v[10:11] op_sel_hi:[1,0]
	v_add_u32_e32 v126, v121, v93
	v_lshl_add_u32 v22, v126, 1, s12
	v_rsq_f32_e32 v13, v13
	v_rsq_f32_e32 v14, v12
	v_mul_f32_e32 v12, 0x3db504f3, v13
	v_pk_mul_f32 v[12:13], v[62:63], v[12:13] op_sel_hi:[1,0]
	v_readlane_b32 s1, v35, 24
	v_cvt_pk_bf16_f32 v12, v12, v13
	v_readlane_b32 s0, v35, 28
	ds_write_b32 v90, v12 offset:34816
	v_pk_mul_f32 v[14:15], v[58:59], v[14:15] op_sel_hi:[1,0]
	v_pk_add_f32 v[12:13], s[0:1], v[10:11] op_sel_hi:[1,0]
	v_cvt_pk_bf16_f32 v36, v14, v15
	v_readlane_b32 s96, v95, s6
	v_rsq_f32_e32 v13, v13
	v_rsq_f32_e32 v18, v12
	v_mul_f32_e32 v12, 0x3db504f3, v13
	v_pk_mul_f32 v[12:13], v[68:69], v[12:13] op_sel_hi:[1,0]
	v_pk_mul_f32 v[18:19], v[66:67], v[18:19] op_sel_hi:[1,0]
	v_cvt_pk_bf16_f32 v12, v12, v13
	v_cvt_pk_bf16_f32 v37, v18, v19
	ds_write_b32 v110, v12 offset:34816
	v_mov_b32_e32 v12, v14
	v_mov_b32_e32 v13, v18
	v_mov_b32_e32 v18, v15
	v_pk_mul_f32 v[12:13], s[82:83], v[12:13]
	v_pk_mul_f32 v[14:15], s[82:83], v[18:19]
	v_pk_mul_f32 v[20:21], s[20:21], v[12:13]
	v_cvt_pk_bf16_f32 v12, v12, v14
	v_pk_mul_f32 v[18:19], s[20:21], v[14:15]
	ds_write2st64_b32 v90, v36, v12 offset1:68
	v_cvt_pk_bf16_f32 v12, v13, v15
	v_cvt_pk_bf16_f32 v20, v20, v21
	ds_write2st64_b32 v110, v37, v12 offset1:68
	ds_write_b32 v88, v84 offset:52228
	ds_write_b32 v85, v20
	ds_write_b32 v82, v115 offset:52228
	v_cvt_pk_bf16_f32 v12, v18, v19
	v_readlane_b32 s1, v35, 32
	v_readlane_b32 s0, v35, 36
	ds_write_b32 v114, v12
	v_readlane_b32 s97, v95, s7
	v_pk_add_f32 v[12:13], s[0:1], v[10:11] op_sel_hi:[1,0]
	v_readlane_b32 s34, v94, s6
	v_readlane_b32 s35, v94, s7
	v_rsq_f32_e32 v13, v13
	v_rsq_f32_e32 v14, v12
	v_mul_f32_e32 v12, 0x3db504f3, v13
	v_pk_mul_f32 v[12:13], v[78:79], v[12:13] op_sel_hi:[1,0]
	v_pk_mul_f32 v[14:15], v[74:75], v[14:15] op_sel_hi:[1,0]
	v_cvt_pk_bf16_f32 v12, v12, v13
	v_readlane_b32 s1, v35, 40
	v_readlane_b32 s0, v35, 44
	v_cvt_pk_bf16_f32 v18, v14, v15
	ds_write_b32 v83, v12 offset:34816
	v_pk_add_f32 v[12:13], s[0:1], v[10:11] op_sel_hi:[1,0]
	ds_write_b32 v83, v18
	s_mov_b64 s[2:3], -1
	v_rsq_f32_e32 v13, v13
	v_rsq_f32_e32 v18, v12
	v_mul_f32_e32 v12, 0x3db504f3, v13
	v_pk_mul_f32 v[12:13], v[80:81], v[12:13] op_sel_hi:[1,0]
	v_pk_mul_f32 v[18:19], v[76:77], v[18:19] op_sel_hi:[1,0]
	v_cvt_pk_bf16_f32 v12, v12, v13
	v_cvt_pk_bf16_f32 v20, v18, v19
	ds_write_b32 v119, v12 offset:34816
	v_mov_b32_e32 v12, v14
	v_mov_b32_e32 v13, v18
	v_mov_b32_e32 v18, v15
	v_pk_mul_f32 v[12:13], s[92:93], v[12:13]
	v_pk_mul_f32 v[14:15], s[92:93], v[18:19]
	ds_write_b32 v119, v20
	v_pk_mul_f32 v[20:21], s[22:23], v[12:13]
	v_cvt_pk_bf16_f32 v12, v12, v14
	v_pk_mul_f32 v[18:19], s[22:23], v[14:15]
	ds_write_b32 v83, v12 offset:17408
	v_cvt_pk_bf16_f32 v12, v13, v15
	v_cvt_pk_bf16_f32 v20, v20, v21
	ds_write_b32 v119, v12 offset:17408
	ds_write_b32 v88, v129 offset:52232
	ds_write_b32 v22, v20
	ds_write_b32 v82, v23 offset:52232
	v_cvt_pk_bf16_f32 v12, v18, v19
	v_readlane_b32 s1, v35, 48
	v_readlane_b32 s0, v35, 52
	ds_write_b32 v32, v12
	s_nop 0
	v_pk_add_f32 v[12:13], s[0:1], v[10:11] op_sel_hi:[1,0]
	s_nop 0
	s_nop 0
	v_rsq_f32_e32 v13, v13
	v_rsq_f32_e32 v14, v12
	v_mul_f32_e32 v12, 0x3db504f3, v13
	v_pk_mul_f32 v[12:13], v[54:55], v[12:13] op_sel_hi:[1,0]
	v_readlane_b32 s1, v35, 56
	v_readlane_b32 s0, v35, 60
	v_cvt_pk_bf16_f32 v12, v12, v13
	ds_write_b32 v33, v12 offset:34816
	v_pk_add_f32 v[10:11], s[0:1], v[10:11] op_sel_hi:[1,0]
	v_pk_mul_f32 v[14:15], v[60:61], v[14:15] op_sel_hi:[1,0]
	v_cvt_pk_bf16_f32 v18, v14, v15
	v_rsq_f32_e32 v11, v11
	v_rsq_f32_e32 v12, v10
	ds_write_b32 v33, v18
	v_mul_f32_e32 v10, 0x3db504f3, v11
	v_pk_mul_f32 v[8:9], v[8:9], v[10:11] op_sel_hi:[1,0]
	v_pk_mul_f32 v[10:11], v[16:17], v[12:13] op_sel_hi:[1,0]
	v_pk_fma_f32 v[16:17], v[226:227], v[72:73], 0 op_sel_hi:[0,1,0]
	v_cvt_pk_bf16_f32 v12, v10, v11
	ds_write_b32 v34, v12
	v_pk_mov_b32 v[12:13], v[28:29], v[30:31] op_sel:[1,0]
	v_pk_fma_f32 v[16:17], v[232:233], v[28:29], v[16:17] op_sel_hi:[0,1,1]
	v_pk_fma_f32 v[12:13], v[240:241], v[12:13], v[16:17] op_sel_hi:[0,1,1]
	v_pk_fma_f32 v[12:13], v[246:247], v[30:31], v[12:13] op_sel_hi:[0,1,1]
	v_mul_f32_e32 v16, 0xbfb8aa3b, v13
	v_exp_f32_e32 v16, v16
	v_mul_f32_e32 v17, 0xbfb8aa3b, v12
	v_exp_f32_e32 v17, v17
	v_cvt_pk_bf16_f32 v18, v8, v9
	v_add_f32_e32 v8, 1.0, v16
	v_rcp_f32_e32 v9, v8
	v_add_f32_e32 v8, 1.0, v17
	v_rcp_f32_e32 v8, v8
	v_pk_fma_f32 v[0:1], v[226:227], v[70:71], 0 op_sel:[1,0,0] op_sel_hi:[1,1,0]
	ds_write_b32 v34, v18 offset:34816
	v_pk_fma_f32 v[0:1], v[232:233], v[24:25], v[0:1] op_sel:[1,0,0]
	v_pk_mul_f32 v[8:9], v[12:13], v[8:9]
	v_pk_mov_b32 v[12:13], v[24:25], v[26:27] op_sel:[1,0]
	v_pk_mul_f32 v[8:9], v[8:9], s[96:97]
	v_pk_fma_f32 v[0:1], v[240:241], v[12:13], v[0:1] op_sel:[1,0,0]
	v_cvt_pk_bf16_f32 v18, v8, v9
	v_pk_fma_f32 v[0:1], v[246:247], v[26:27], v[0:1] op_sel:[1,0,0]
	v_mov_b32_e32 v8, v14
	v_mul_f32_e32 v2, 0xbfb8aa3b, v1
	v_exp_f32_e32 v4, v2
	v_mul_f32_e32 v2, 0xbfb8aa3b, v0
	v_exp_f32_e32 v6, v2
	v_mov_b32_e32 v9, v10
	v_add_f32_e32 v4, 1.0, v4
	v_rcp_f32_e32 v5, v4
	v_add_f32_e32 v4, 1.0, v6
	v_rcp_f32_e32 v4, v4
	v_pk_mul_f32 v[8:9], s[96:97], v[8:9]
	v_mov_b32_e32 v10, v15
	v_pk_mul_f32 v[2:3], s[34:35], v[8:9]
	v_pk_mul_f32 v[0:1], v[0:1], v[4:5]
	v_or_b32_e32 v16, 6, v92
	v_pk_mul_f32 v[0:1], v[0:1], s[96:97]
	v_cvt_pk_bf16_f32 v6, v2, v3
	v_cvt_pk_bf16_f32 v4, v0, v1
	v_pk_mul_f32 v[0:1], s[96:97], v[10:11]
	v_add_u32_e32 v17, v16, v93
	v_pk_mul_f32 v[2:3], s[34:35], v[0:1]
	v_cvt_pk_bf16_f32 v0, v8, v0
	v_add_u32_e32 v12, v16, v89
	ds_write_b32 v33, v0 offset:17408
	v_cvt_pk_bf16_f32 v0, v9, v1
	v_lshl_add_u32 v7, v17, 1, s12
	ds_write_b32 v34, v0 offset:17408
	ds_write_b32 v88, v18 offset:52236
	ds_write_b32 v7, v6
	ds_write_b32 v82, v4 offset:52236
	v_cvt_pk_bf16_f32 v0, v2, v3
	v_lshl_add_u32 v1, v12, 1, s12
	ds_write_b32 v1, v0
	s_waitcnt lgkmcnt(0)
	s_barrier
	s_cmp_lg_u32 s95, 0
	s_cbranch_scc1 .Lgpf_done_next
	v_readlane_b32 s99, v253, 10
	s_nop 0
	s_add_i32 s99, s76, s99
	s_cmpk_lt_i32 s99, 0x800
	s_cbranch_scc0 .Lgpf_done_next
	v_readlane_b32 s100, v253, 17
	s_lshr_b32 s0, s99, 8
	s_lshl_b32 s0, s0, 12
	s_and_b32 s1, s99, 63
	s_lshl_b32 s101, s1, 6
	s_add_i32 s0, s0, s101
	s_or_b32 s1, s1, s100
	s_bfe_u32 s101, s99, 0x20006
	v_add_u32_e32 v219, s0, v237
	v_lshlrev_b32_e32 v219, 5, v219
	s_lshl_b32 s99, s101, 2
	v_add_u32_e32 v219, s99, v219
	s_lshl_b32 s100, s100, 3
	s_add_i32 s0, s0, s100
	s_lshl_b32 s0, s0, 10
	s_lshl_b32 s101, s101, 8
	s_add_i32 s0, s0, s101
	v_lshlrev_b32_e32 v217, 2, v237
	v_add_u32_e32 v217, s0, v217
	v_add_u32_e32 v218, 0x1000, v217
	s_add_u32 s100, s88, 0x200000
	s_addc_u32 s101, s89, 0
	s_cmp_eq_u32 s1, 0
	s_cbranch_scc1 .Lgpf_zero_next
	global_load_dword v172, v217, s[44:45] offset:-3072 nt
	global_load_dword v173, v217, s[68:69] offset:-3072 nt
	global_load_dword v174, v217, s[72:73] offset:-3072 nt
	global_load_dword v175, v217, s[44:45] offset:-2048 nt
	global_load_dword v176, v217, s[68:69] offset:-2048 nt
	global_load_dword v177, v217, s[72:73] offset:-2048 nt
	global_load_dword v178, v217, s[44:45] offset:-1024 nt
	global_load_dword v179, v217, s[68:69] offset:-1024 nt
	global_load_dword v180, v217, s[72:73] offset:-1024 nt
	s_branch .Lgpf_rest_next
